# attention main loop: m0 save/restore around LDS-DMA loads and add of zero removed
# baseline (speedup 1.0000x reference)
.LBB0_1028:
	v_add_u32_e32 v230, s44, v243
	ds_read_b64_tr_b16 v[190:191], v230 offset:49152
	ds_read_b64_tr_b16 v[192:193], v230 offset:49664
	s_waitcnt lgkmcnt(9)
	v_mfma_f32_32x32x16_bf16 v[114:129], v[102:105], v[158:161], 0
	v_add_f32_e32 v106, v82, v83
	v_add_f32_e32 v106, v84, v106
	v_add_f32_e32 v106, v85, v106
	v_add_f32_e32 v106, v86, v106
	v_add_f32_e32 v106, v87, v106
	v_cvt_pk_bf16_f32 v150, v82, v83
	v_cvt_pk_bf16_f32 v151, v84, v85
	ds_read_b64_tr_b16 v[186:187], v230 offset:53248
	ds_read_b64_tr_b16 v[188:189], v230 offset:53760
	v_add_f32_e32 v82, v88, v106
	s_waitcnt lgkmcnt(10)
	v_mfma_f32_32x32x16_bf16 v[98:113], v[98:101], v[158:161], 0
	v_add_f32_e32 v82, v89, v82
	v_add_f32_e32 v82, v90, v82
	v_add_f32_e32 v130, v91, v82
	v_cvt_pk_bf16_f32 v152, v86, v87
	v_cvt_pk_bf16_f32 v153, v88, v89
	ds_read_b64_tr_b16 v[82:83], v230 offset:57344
	ds_read_b64_tr_b16 v[84:85], v230 offset:57856
	s_waitcnt lgkmcnt(11)
	v_mfma_f32_32x32x16_bf16 v[114:129], v[182:185], v[154:157], v[114:129]
	v_add_f32_e32 v86, v92, v130
	v_add_f32_e32 v86, v93, v86
	v_add_f32_e32 v86, v94, v86
	v_add_f32_e32 v130, v95, v86
	v_cvt_pk_bf16_f32 v138, v90, v91
	v_cvt_pk_bf16_f32 v139, v92, v93
	ds_read_b64_tr_b16 v[86:87], v230 offset:61440
	ds_read_b64_tr_b16 v[88:89], v230 offset:61952
	s_waitcnt lgkmcnt(12)
	v_mfma_f32_32x32x16_bf16 v[98:113], v[178:181], v[154:157], v[98:113]
	v_add_f32_e32 v90, v96, v130
	v_add_f32_e32 v90, v97, v90
	v_add_f32_e32 v90, v66, v90
	v_add_f32_e32 v130, v67, v90
	v_cvt_pk_bf16_f32 v140, v94, v95
	v_cvt_pk_bf16_f32 v141, v96, v97
	ds_read_b64_tr_b16 v[90:91], v230 offset:50176
	ds_read_b64_tr_b16 v[92:93], v230 offset:50688
	s_waitcnt lgkmcnt(13)
	v_mfma_f32_32x32x16_bf16 v[114:129], v[174:177], v[146:149], v[114:129]
	v_add_f32_e32 v94, v68, v130
	v_add_f32_e32 v94, v69, v94
	v_add_f32_e32 v94, v70, v94
	v_add_f32_e32 v130, v71, v94
	v_cvt_pk_bf16_f32 v134, v66, v67
	v_cvt_pk_bf16_f32 v135, v68, v69
	ds_read_b64_tr_b16 v[94:95], v230 offset:54272
	ds_read_b64_tr_b16 v[96:97], v230 offset:54784
	s_waitcnt lgkmcnt(14)
	v_mfma_f32_32x32x16_bf16 v[98:113], v[170:173], v[146:149], v[98:113]
	v_add_f32_e32 v66, v72, v130
	v_add_f32_e32 v66, v73, v66
	v_add_f32_e32 v66, v74, v66
	v_add_f32_e32 v66, v75, v66
	v_cvt_pk_bf16_f32 v136, v70, v71
	v_cvt_pk_bf16_f32 v137, v72, v73
	ds_read_b64_tr_b16 v[194:195], v230 offset:58368
	ds_read_b64_tr_b16 v[196:197], v230 offset:58880
	s_waitcnt lgkmcnt(14)
	v_mfma_f32_32x32x16_bf16 v[114:129], v[166:169], v[142:145], v[114:129]
	v_add_f32_e32 v66, v76, v66
	v_add_f32_e32 v66, v77, v66
	v_add_f32_e32 v66, v78, v66
	v_add_f32_e32 v66, v79, v66
	v_cvt_pk_bf16_f32 v130, v74, v75
	v_cvt_pk_bf16_f32 v131, v76, v77
	ds_read_b64_tr_b16 v[74:75], v230 offset:62464
	ds_read_b64_tr_b16 v[76:77], v230 offset:62976
	v_mfma_f32_32x32x16_bf16 v[98:113], v[162:165], v[142:145], v[98:113]
	v_add_f32_e32 v66, v80, v66
	v_add_f32_e32 v66, v81, v66
	v_cvt_pk_bf16_f32 v132, v78, v79
	v_cvt_pk_bf16_f32 v133, v80, v81
	s_add_i32 s4, s10, s89
	s_mov_b32 m0, s4
	s_nop 0
	global_load_lds_dwordx4 v[220:221], off
	v_add_f32_e32 v234, v234, v66
	s_addk_i32 s4, 0x400
	s_mov_b32 m0, s4
	s_nop 0
	global_load_lds_dwordx4 v[218:219], off
	v_lshl_add_u64 v[66:67], v[224:225], 0, s[0:1]
	s_add_i32 s4, s9, s70
	s_mov_b32 m0, s4
	s_nop 0
	global_load_lds_dwordx4 v[66:67], off
	v_lshl_add_u64 v[66:67], v[224:225], 0, s[64:65]
	s_addk_i32 s4, 0x400
	s_mov_b32 m0, s4
	s_nop 0
	global_load_lds_dwordx4 v[66:67], off
	v_max_f32_e32 v66, v115, v115
	v_max_f32_e32 v67, v114, v114
	v_max_f32_e32 v66, v67, v66
	v_max3_f32 v67, v116, v117, v99
	v_max3_f32 v66, v66, v98, v100
	v_max3_f32 v66, v66, v101, v118
	v_max3_f32 v67, v67, v120, v121
	v_max3_f32 v66, v66, v119, v102
	v_max3_f32 v67, v67, v104, v105
	v_max3_f32 v66, v66, v103, v122
	v_max3_f32 v67, v67, v124, v125
	v_max3_f32 v66, v66, v123, v106
	v_max3_f32 v67, v67, v108, v109
	v_max3_f32 v66, v66, v107, v126
	v_max3_f32 v67, v67, v128, v129
	v_max3_f32 v66, v66, v127, v110
	v_max3_f32 v67, v67, v112, v113
	v_max3_f32 v66, v66, v111, v67
	v_mov_b32_e32 v67, v66
	s_nop 1
	v_permlane32_swap_b32_e32 v66, v67
	v_max_f32_e32 v67, v67, v67
	v_max_f32_e32 v66, v66, v66
	v_max_f32_e32 v66, v66, v67
	v_sub_f32_e32 v66, v66, v207
	v_cmp_lt_f32_e32 vcc, s3, v66
	s_cmp_lg_u64 vcc, 0
	s_cselect_b64 s[4:5], -1, 0
	s_cbranch_vccnz .LBB0_1036

.LBB0_1031:
	s_add_i32 s4, s9, 0x4000
	s_cmpk_lg_u32 s9, 0x8000
	s_cselect_b32 s11, s4, 0
	v_add_u32_e32 v230, s10, v243
	ds_read_b64_tr_b16 v[190:191], v230 offset:49152
	ds_read_b64_tr_b16 v[192:193], v230 offset:49664
	v_mfma_f32_32x32x16_bf16 v[82:97], v[70:73], v[158:161], 0
	v_add_f32_e32 v74, v114, v115
	v_add_f32_e32 v74, v116, v74
	v_add_f32_e32 v74, v117, v74
	v_add_f32_e32 v74, v118, v74
	v_add_f32_e32 v74, v119, v74
	v_cvt_pk_bf16_f32 v150, v114, v115
	v_cvt_pk_bf16_f32 v151, v116, v117
	ds_read_b64_tr_b16 v[186:187], v230 offset:53248
	ds_read_b64_tr_b16 v[188:189], v230 offset:53760
	v_add_f32_e32 v70, v120, v74
	v_add_f32_e32 v70, v121, v70
	v_add_f32_e32 v70, v122, v70
	v_add_f32_e32 v130, v123, v70
	v_mfma_f32_32x32x16_bf16 v[66:81], v[66:69], v[158:161], 0
	v_cvt_pk_bf16_f32 v152, v118, v119
	v_cvt_pk_bf16_f32 v153, v120, v121
	ds_read_b64_tr_b16 v[114:115], v230 offset:57344
	ds_read_b64_tr_b16 v[116:117], v230 offset:57856
	v_mfma_f32_32x32x16_bf16 v[82:97], v[182:185], v[154:157], v[82:97]
	v_add_f32_e32 v118, v124, v130
	v_add_f32_e32 v118, v125, v118
	v_add_f32_e32 v118, v126, v118
	v_add_f32_e32 v130, v127, v118
	v_cvt_pk_bf16_f32 v138, v122, v123
	v_cvt_pk_bf16_f32 v139, v124, v125
	ds_read_b64_tr_b16 v[118:119], v230 offset:61440
	ds_read_b64_tr_b16 v[120:121], v230 offset:61952
	v_mfma_f32_32x32x16_bf16 v[66:81], v[178:181], v[154:157], v[66:81]
	v_add_f32_e32 v122, v128, v130
	v_add_f32_e32 v122, v129, v122
	v_add_f32_e32 v122, v98, v122
	v_add_f32_e32 v130, v99, v122
	v_cvt_pk_bf16_f32 v140, v126, v127
	v_cvt_pk_bf16_f32 v141, v128, v129
	ds_read_b64_tr_b16 v[122:123], v230 offset:50176
	ds_read_b64_tr_b16 v[124:125], v230 offset:50688
	v_mfma_f32_32x32x16_bf16 v[82:97], v[174:177], v[146:149], v[82:97]
	v_add_f32_e32 v126, v100, v130
	v_add_f32_e32 v126, v101, v126
	v_add_f32_e32 v126, v102, v126
	v_add_f32_e32 v130, v103, v126
	v_cvt_pk_bf16_f32 v134, v98, v99
	v_cvt_pk_bf16_f32 v135, v100, v101
	ds_read_b64_tr_b16 v[126:127], v230 offset:54272
	ds_read_b64_tr_b16 v[128:129], v230 offset:54784
	v_mfma_f32_32x32x16_bf16 v[66:81], v[170:173], v[146:149], v[66:81]
	v_add_f32_e32 v98, v104, v130
	v_add_f32_e32 v98, v105, v98
	v_add_f32_e32 v98, v106, v98
	v_add_f32_e32 v98, v107, v98
	v_cvt_pk_bf16_f32 v136, v102, v103
	v_cvt_pk_bf16_f32 v137, v104, v105
	ds_read_b64_tr_b16 v[194:195], v230 offset:58368
	ds_read_b64_tr_b16 v[196:197], v230 offset:58880
	v_mfma_f32_32x32x16_bf16 v[82:97], v[166:169], v[142:145], v[82:97]
	v_add_f32_e32 v98, v108, v98
	v_add_f32_e32 v98, v109, v98
	v_add_f32_e32 v98, v110, v98
	v_add_f32_e32 v98, v111, v98
	v_cvt_pk_bf16_f32 v130, v106, v107
	v_cvt_pk_bf16_f32 v131, v108, v109
	ds_read_b64_tr_b16 v[106:107], v230 offset:62464
	ds_read_b64_tr_b16 v[108:109], v230 offset:62976
	v_mfma_f32_32x32x16_bf16 v[66:81], v[162:165], v[142:145], v[66:81]
	v_add_f32_e32 v98, v112, v98
	v_add_f32_e32 v98, v113, v98
	v_cvt_pk_bf16_f32 v132, v110, v111
	v_cvt_pk_bf16_f32 v133, v112, v113
	s_nop 0
	v_add_f32_e32 v234, v234, v98
	s_add_i32 s4, s9, s89
	v_lshl_add_u64 v[98:99], v[220:221], 0, s[0:1]
	s_mov_b32 m0, s4
	s_nop 0
	global_load_lds_dwordx4 v[98:99], off
	v_lshl_add_u64 v[98:99], v[218:219], 0, s[0:1]
	s_addk_i32 s4, 0x400
	s_mov_b32 m0, s4
	s_nop 0
	global_load_lds_dwordx4 v[98:99], off
	v_lshl_add_u64 v[110:111], v[224:225], 0, s[74:75]
	s_add_i32 s4, s11, s70
	s_mov_b32 m0, s4
	s_nop 0
	global_load_lds_dwordx4 v[110:111], off
	v_lshl_add_u64 v[98:99], v[224:225], 0, s[62:63]
	s_addk_i32 s4, 0x400
	s_mov_b32 m0, s4
	s_nop 0
	global_load_lds_dwordx4 v[98:99], off
	v_max_f32_e32 v98, v83, v83
	v_max_f32_e32 v99, v82, v82
	v_max_f32_e32 v98, v99, v98
	v_max3_f32 v99, v84, v85, v67
	v_max3_f32 v98, v98, v66, v68
	v_max3_f32 v98, v98, v69, v86
	v_max3_f32 v99, v99, v88, v89
	v_max3_f32 v98, v98, v87, v70
	v_max3_f32 v99, v99, v72, v73
	v_max3_f32 v98, v98, v71, v90
	v_max3_f32 v99, v99, v92, v93
	v_max3_f32 v98, v98, v91, v74
	v_max3_f32 v99, v99, v76, v77
	v_max3_f32 v98, v98, v75, v94
	v_max3_f32 v99, v99, v96, v97
	v_max3_f32 v98, v98, v95, v78
	v_max3_f32 v99, v99, v80, v81
	v_max3_f32 v98, v98, v79, v99
	v_mov_b32_e32 v99, v98
	s_nop 1
	v_permlane32_swap_b32_e32 v98, v99
	v_max_f32_e32 v99, v99, v99
	v_max_f32_e32 v98, v98, v98
	v_max_f32_e32 v98, v98, v99
	v_sub_f32_e32 v98, v98, v207
	v_cmp_lt_f32_e32 vcc, s3, v98
	s_cmp_lg_u64 vcc, 0
	s_cselect_b64 s[4:5], -1, 0
	s_cbranch_vccnz .LBB0_1039
